# prep_all: 32 long-latency column-sum blocks remapped to run first (block ids 0..31) instead of last; on top of KV2 epilogue rewrite
# speedup vs baseline: 1.0255x; 1.0255x over previous
_Z8prep_all5PArgs:
	s_add_i32 s3, s2, 0x1a01
	s_sub_i32 s4, s2, 32
	s_cmp_lt_u32 s2, 32
	s_cselect_b32 s2, s3, s4
	s_cmpk_gt_i32 s2, 0xfff
	s_mov_b64 s[4:5], -1
	s_cbranch_scc1 .LBB0_3
	s_andn2_b64 vcc, exec, s[4:5]
	s_cbranch_vccz .LBB0_40
